# baseline (speedup 1.0000x reference)
.Lup_loop:
	s_waitcnt lgkmcnt(0)
	v_mfma_f32_16x16x32_bf16 v[128:131], v[48:51], v[32:35], v[128:131]
	ds_read_b128 v[80:83], v13 offset:0
	v_mfma_f32_16x16x32_bf16 v[132:135], v[48:51], v[36:39], v[132:135]
	s_add_u32 m0, s20, 0x6000
	v_mfma_f32_16x16x32_bf16 v[136:139], v[48:51], v[40:43], v[136:139]
	ds_read_b128 v[84:87], v13 offset:2048
	v_mfma_f32_16x16x32_bf16 v[140:143], v[48:51], v[44:47], v[140:143]
	global_load_lds_dwordx4 v4, s[18:19]
	v_mfma_f32_16x16x32_bf16 v[144:147], v[52:55], v[32:35], v[144:147]
	ds_read_b128 v[88:91], v13 offset:4096
	v_mfma_f32_16x16x32_bf16 v[148:151], v[52:55], v[36:39], v[148:151]
	s_add_u32 m0, s20, 0x7000
	v_mfma_f32_16x16x32_bf16 v[152:155], v[52:55], v[40:43], v[152:155]
	ds_read_b128 v[92:95], v13 offset:6144
	v_mfma_f32_16x16x32_bf16 v[156:159], v[52:55], v[44:47], v[156:159]
	global_load_lds_dwordx4 v5, s[18:19]
	v_mfma_f32_16x16x32_bf16 v[160:163], v[56:59], v[32:35], v[160:163]
	ds_read_b128 v[96:99], v15 offset:0
	v_mfma_f32_16x16x32_bf16 v[164:167], v[56:59], v[36:39], v[164:167]
	s_add_u32 m0, s20, 0x8000
	v_mfma_f32_16x16x32_bf16 v[168:171], v[56:59], v[40:43], v[168:171]
	ds_read_b128 v[100:103], v15 offset:2048
	v_mfma_f32_16x16x32_bf16 v[172:175], v[56:59], v[44:47], v[172:175]
	global_load_lds_dwordx4 v6, s[18:19]
	v_mfma_f32_16x16x32_bf16 v[176:179], v[60:63], v[32:35], v[176:179]
	ds_read_b128 v[104:107], v15 offset:4096
	v_mfma_f32_16x16x32_bf16 v[180:183], v[60:63], v[36:39], v[180:183]
	s_add_u32 m0, s20, 0x9000
	v_mfma_f32_16x16x32_bf16 v[184:187], v[60:63], v[40:43], v[184:187]
	ds_read_b128 v[108:111], v15 offset:6144
	v_mfma_f32_16x16x32_bf16 v[188:191], v[60:63], v[44:47], v[188:191]
	global_load_lds_dwordx4 v7, s[18:19]
	v_mfma_f32_16x16x32_bf16 v[192:195], v[64:67], v[32:35], v[192:195]
	ds_read_b128 v[112:115], v15 offset:8192
	v_mfma_f32_16x16x32_bf16 v[196:199], v[64:67], v[36:39], v[196:199]
	s_add_u32 m0, s20, 0xa000
	v_mfma_f32_16x16x32_bf16 v[200:203], v[64:67], v[40:43], v[200:203]
	ds_read_b128 v[116:119], v15 offset:10240
	v_mfma_f32_16x16x32_bf16 v[204:207], v[64:67], v[44:47], v[204:207]
	global_load_lds_dwordx4 v8, s[18:19]
	v_mfma_f32_16x16x32_bf16 v[208:211], v[68:71], v[32:35], v[208:211]
	ds_read_b128 v[120:123], v15 offset:12288
	v_mfma_f32_16x16x32_bf16 v[212:215], v[68:71], v[36:39], v[212:215]
	s_add_u32 m0, s20, 0xb000
	v_mfma_f32_16x16x32_bf16 v[216:219], v[68:71], v[40:43], v[216:219]
	ds_read_b128 v[124:127], v15 offset:14336
	v_mfma_f32_16x16x32_bf16 v[220:223], v[68:71], v[44:47], v[220:223]
	global_load_lds_dwordx4 v9, s[18:19]
	v_mfma_f32_16x16x32_bf16 v[224:227], v[72:75], v[32:35], v[224:227]
	v_mfma_f32_16x16x32_bf16 v[228:231], v[72:75], v[36:39], v[228:231]
	v_mfma_f32_16x16x32_bf16 v[232:235], v[72:75], v[40:43], v[232:235]
	v_mfma_f32_16x16x32_bf16 v[236:239], v[72:75], v[44:47], v[236:239]
	v_mfma_f32_16x16x32_bf16 v[240:243], v[76:79], v[32:35], v[240:243]
	s_add_u32 s16, s16, 0x80
	s_addc_u32 s17, s17, 0
	s_add_u32 s18, s18, 0x80
	s_addc_u32 s19, s19, 0
	v_mfma_f32_16x16x32_bf16 v[244:247], v[76:79], v[36:39], v[244:247]
	s_add_u32 s20, s20, 0xc000
	s_sub_u32 s22, s20, 0x24000
	s_cmp_ge_u32 s20, 0x24000
	s_cselect_b32 s20, s22, s20
	v_mfma_f32_16x16x32_bf16 v[248:251], v[76:79], v[40:43], v[248:251]
	v_add_u32_e32 v12, s21, v10
	v_add_u32_e32 v14, s21, v11
	v_xor_b32_e32 v13, 64, v12
	v_xor_b32_e32 v15, 64, v14
	v_mfma_f32_16x16x32_bf16 v[252:255], v[76:79], v[44:47], v[252:255]
	s_add_u32 s21, s21, 0xc000
	s_sub_u32 s23, s21, 0x24000
	s_cmp_ge_u32 s21, 0x24000
	s_cselect_b32 s21, s23, s21
	s_waitcnt lgkmcnt(0)
	v_mfma_f32_16x16x32_bf16 v[128:131], v[96:99], v[80:83], v[128:131]
	v_mfma_f32_16x16x32_bf16 v[132:135], v[96:99], v[84:87], v[132:135]
	v_mfma_f32_16x16x32_bf16 v[136:139], v[96:99], v[88:91], v[136:139]
	v_mfma_f32_16x16x32_bf16 v[140:143], v[96:99], v[92:95], v[140:143]
	v_mfma_f32_16x16x32_bf16 v[144:147], v[100:103], v[80:83], v[144:147]
	v_mfma_f32_16x16x32_bf16 v[148:151], v[100:103], v[84:87], v[148:151]
	v_mfma_f32_16x16x32_bf16 v[152:155], v[100:103], v[88:91], v[152:155]
	v_mfma_f32_16x16x32_bf16 v[156:159], v[100:103], v[92:95], v[156:159]
	s_waitcnt vmcnt(12)
	s_barrier
	v_mfma_f32_16x16x32_bf16 v[160:163], v[104:107], v[80:83], v[160:163]
	ds_read_b128 v[32:35], v12 offset:0
	v_mfma_f32_16x16x32_bf16 v[164:167], v[104:107], v[84:87], v[164:167]
	s_add_u32 m0, s20, 0x0
	v_mfma_f32_16x16x32_bf16 v[168:171], v[104:107], v[88:91], v[168:171]
	ds_read_b128 v[36:39], v12 offset:2048
	v_mfma_f32_16x16x32_bf16 v[172:175], v[104:107], v[92:95], v[172:175]
	global_load_lds_dwordx4 v2, s[16:17]
	v_mfma_f32_16x16x32_bf16 v[176:179], v[108:111], v[80:83], v[176:179]
	ds_read_b128 v[40:43], v12 offset:4096
	v_mfma_f32_16x16x32_bf16 v[180:183], v[108:111], v[84:87], v[180:183]
	s_add_u32 m0, s20, 0x1000
	v_mfma_f32_16x16x32_bf16 v[184:187], v[108:111], v[88:91], v[184:187]
	ds_read_b128 v[44:47], v12 offset:6144
	v_mfma_f32_16x16x32_bf16 v[188:191], v[108:111], v[92:95], v[188:191]
	global_load_lds_dwordx4 v3, s[16:17]
	v_mfma_f32_16x16x32_bf16 v[192:195], v[112:115], v[80:83], v[192:195]
	ds_read_b128 v[48:51], v14 offset:0
	v_mfma_f32_16x16x32_bf16 v[196:199], v[112:115], v[84:87], v[196:199]
	s_add_u32 m0, s20, 0x2000
	v_mfma_f32_16x16x32_bf16 v[200:203], v[112:115], v[88:91], v[200:203]
	ds_read_b128 v[52:55], v14 offset:2048
	v_mfma_f32_16x16x32_bf16 v[204:207], v[112:115], v[92:95], v[204:207]
	global_load_lds_dwordx4 v4, s[16:17]
	v_mfma_f32_16x16x32_bf16 v[208:211], v[116:119], v[80:83], v[208:211]
	ds_read_b128 v[56:59], v14 offset:4096
	v_mfma_f32_16x16x32_bf16 v[212:215], v[116:119], v[84:87], v[212:215]
	s_add_u32 m0, s20, 0x3000
	v_mfma_f32_16x16x32_bf16 v[216:219], v[116:119], v[88:91], v[216:219]
	ds_read_b128 v[60:63], v14 offset:6144
	v_mfma_f32_16x16x32_bf16 v[220:223], v[116:119], v[92:95], v[220:223]
	global_load_lds_dwordx4 v5, s[16:17]
	v_mfma_f32_16x16x32_bf16 v[224:227], v[120:123], v[80:83], v[224:227]
	ds_read_b128 v[64:67], v14 offset:8192
	v_mfma_f32_16x16x32_bf16 v[228:231], v[120:123], v[84:87], v[228:231]
	s_add_u32 m0, s20, 0x4000
	v_mfma_f32_16x16x32_bf16 v[232:235], v[120:123], v[88:91], v[232:235]
	ds_read_b128 v[68:71], v14 offset:10240
	v_mfma_f32_16x16x32_bf16 v[236:239], v[120:123], v[92:95], v[236:239]
	global_load_lds_dwordx4 v2, s[18:19]
	v_mfma_f32_16x16x32_bf16 v[240:243], v[124:127], v[80:83], v[240:243]
	ds_read_b128 v[72:75], v14 offset:12288
	v_mfma_f32_16x16x32_bf16 v[244:247], v[124:127], v[84:87], v[244:247]
	s_add_u32 m0, s20, 0x5000
	v_mfma_f32_16x16x32_bf16 v[248:251], v[124:127], v[88:91], v[248:251]
	ds_read_b128 v[76:79], v14 offset:14336
	v_mfma_f32_16x16x32_bf16 v[252:255], v[124:127], v[92:95], v[252:255]
	global_load_lds_dwordx4 v3, s[18:19]
	s_add_u32 s15, s15, 1
	s_cmp_lt_u32 s15, 9
	s_cbranch_scc1 .Lup_loop
	s_waitcnt lgkmcnt(0)
	v_mfma_f32_16x16x32_bf16 v[128:131], v[48:51], v[32:35], v[128:131]
	ds_read_b128 v[80:83], v13 offset:0
	v_mfma_f32_16x16x32_bf16 v[132:135], v[48:51], v[36:39], v[132:135]
	s_add_u32 m0, s20, 0x6000
	v_mfma_f32_16x16x32_bf16 v[136:139], v[48:51], v[40:43], v[136:139]
	ds_read_b128 v[84:87], v13 offset:2048
	v_mfma_f32_16x16x32_bf16 v[140:143], v[48:51], v[44:47], v[140:143]
	global_load_lds_dwordx4 v4, s[18:19]
	v_mfma_f32_16x16x32_bf16 v[144:147], v[52:55], v[32:35], v[144:147]
	ds_read_b128 v[88:91], v13 offset:4096
	v_mfma_f32_16x16x32_bf16 v[148:151], v[52:55], v[36:39], v[148:151]
	s_add_u32 m0, s20, 0x7000
	v_mfma_f32_16x16x32_bf16 v[152:155], v[52:55], v[40:43], v[152:155]
	ds_read_b128 v[92:95], v13 offset:6144
	v_mfma_f32_16x16x32_bf16 v[156:159], v[52:55], v[44:47], v[156:159]
	global_load_lds_dwordx4 v5, s[18:19]
	v_mfma_f32_16x16x32_bf16 v[160:163], v[56:59], v[32:35], v[160:163]
	ds_read_b128 v[96:99], v15 offset:0
	v_mfma_f32_16x16x32_bf16 v[164:167], v[56:59], v[36:39], v[164:167]
	s_add_u32 m0, s20, 0x8000
	v_mfma_f32_16x16x32_bf16 v[168:171], v[56:59], v[40:43], v[168:171]
	ds_read_b128 v[100:103], v15 offset:2048
	v_mfma_f32_16x16x32_bf16 v[172:175], v[56:59], v[44:47], v[172:175]
	global_load_lds_dwordx4 v6, s[18:19]
	v_mfma_f32_16x16x32_bf16 v[176:179], v[60:63], v[32:35], v[176:179]
	ds_read_b128 v[104:107], v15 offset:4096
	v_mfma_f32_16x16x32_bf16 v[180:183], v[60:63], v[36:39], v[180:183]
	s_add_u32 m0, s20, 0x9000
	v_mfma_f32_16x16x32_bf16 v[184:187], v[60:63], v[40:43], v[184:187]
	ds_read_b128 v[108:111], v15 offset:6144
	v_mfma_f32_16x16x32_bf16 v[188:191], v[60:63], v[44:47], v[188:191]
	global_load_lds_dwordx4 v7, s[18:19]
	v_mfma_f32_16x16x32_bf16 v[192:195], v[64:67], v[32:35], v[192:195]
	ds_read_b128 v[112:115], v15 offset:8192
	v_mfma_f32_16x16x32_bf16 v[196:199], v[64:67], v[36:39], v[196:199]
	s_add_u32 m0, s20, 0xa000
	v_mfma_f32_16x16x32_bf16 v[200:203], v[64:67], v[40:43], v[200:203]
	ds_read_b128 v[116:119], v15 offset:10240
	v_mfma_f32_16x16x32_bf16 v[204:207], v[64:67], v[44:47], v[204:207]
	global_load_lds_dwordx4 v8, s[18:19]
	v_mfma_f32_16x16x32_bf16 v[208:211], v[68:71], v[32:35], v[208:211]
	ds_read_b128 v[120:123], v15 offset:12288
	v_mfma_f32_16x16x32_bf16 v[212:215], v[68:71], v[36:39], v[212:215]
	s_add_u32 m0, s20, 0xb000
	v_mfma_f32_16x16x32_bf16 v[216:219], v[68:71], v[40:43], v[216:219]
	ds_read_b128 v[124:127], v15 offset:14336
	v_mfma_f32_16x16x32_bf16 v[220:223], v[68:71], v[44:47], v[220:223]
	global_load_lds_dwordx4 v9, s[18:19]
	v_mfma_f32_16x16x32_bf16 v[224:227], v[72:75], v[32:35], v[224:227]
	v_mfma_f32_16x16x32_bf16 v[228:231], v[72:75], v[36:39], v[228:231]
	v_mfma_f32_16x16x32_bf16 v[232:235], v[72:75], v[40:43], v[232:235]
	v_mfma_f32_16x16x32_bf16 v[236:239], v[72:75], v[44:47], v[236:239]
	v_mfma_f32_16x16x32_bf16 v[240:243], v[76:79], v[32:35], v[240:243]
	s_add_u32 s16, s16, 0x80
	s_addc_u32 s17, s17, 0
	s_add_u32 s18, s18, 0x80
	s_addc_u32 s19, s19, 0
	v_mfma_f32_16x16x32_bf16 v[244:247], v[76:79], v[36:39], v[244:247]
	s_add_u32 s20, s20, 0xc000
	s_sub_u32 s22, s20, 0x24000
	s_cmp_ge_u32 s20, 0x24000
	s_cselect_b32 s20, s22, s20
	v_mfma_f32_16x16x32_bf16 v[248:251], v[76:79], v[40:43], v[248:251]
	v_add_u32_e32 v12, s21, v10
	v_add_u32_e32 v14, s21, v11
	v_xor_b32_e32 v13, 64, v12
	v_xor_b32_e32 v15, 64, v14
	v_mfma_f32_16x16x32_bf16 v[252:255], v[76:79], v[44:47], v[252:255]
	s_add_u32 s21, s21, 0xc000
	s_sub_u32 s23, s21, 0x24000
	s_cmp_ge_u32 s21, 0x24000
	s_cselect_b32 s21, s23, s21
	s_waitcnt lgkmcnt(0)
	v_mfma_f32_16x16x32_bf16 v[128:131], v[96:99], v[80:83], v[128:131]
	v_mfma_f32_16x16x32_bf16 v[132:135], v[96:99], v[84:87], v[132:135]
	v_mfma_f32_16x16x32_bf16 v[136:139], v[96:99], v[88:91], v[136:139]
	v_mfma_f32_16x16x32_bf16 v[140:143], v[96:99], v[92:95], v[140:143]
	v_mfma_f32_16x16x32_bf16 v[144:147], v[100:103], v[80:83], v[144:147]
	v_mfma_f32_16x16x32_bf16 v[148:151], v[100:103], v[84:87], v[148:151]
	v_mfma_f32_16x16x32_bf16 v[152:155], v[100:103], v[88:91], v[152:155]
	v_mfma_f32_16x16x32_bf16 v[156:159], v[100:103], v[92:95], v[156:159]
	s_waitcnt vmcnt(12)
	s_barrier
	v_mfma_f32_16x16x32_bf16 v[160:163], v[104:107], v[80:83], v[160:163]
	ds_read_b128 v[32:35], v12 offset:0
	v_mfma_f32_16x16x32_bf16 v[164:167], v[104:107], v[84:87], v[164:167]
	ds_read_b128 v[36:39], v12 offset:2048
	v_mfma_f32_16x16x32_bf16 v[168:171], v[104:107], v[88:91], v[168:171]
	ds_read_b128 v[40:43], v12 offset:4096
	v_mfma_f32_16x16x32_bf16 v[172:175], v[104:107], v[92:95], v[172:175]
	ds_read_b128 v[44:47], v12 offset:6144
	v_mfma_f32_16x16x32_bf16 v[176:179], v[108:111], v[80:83], v[176:179]
	ds_read_b128 v[48:51], v14 offset:0
	v_mfma_f32_16x16x32_bf16 v[180:183], v[108:111], v[84:87], v[180:183]
	ds_read_b128 v[52:55], v14 offset:2048
	v_mfma_f32_16x16x32_bf16 v[184:187], v[108:111], v[88:91], v[184:187]
	ds_read_b128 v[56:59], v14 offset:4096
	v_mfma_f32_16x16x32_bf16 v[188:191], v[108:111], v[92:95], v[188:191]
	ds_read_b128 v[60:63], v14 offset:6144
	v_mfma_f32_16x16x32_bf16 v[192:195], v[112:115], v[80:83], v[192:195]
	ds_read_b128 v[64:67], v14 offset:8192
	v_mfma_f32_16x16x32_bf16 v[196:199], v[112:115], v[84:87], v[196:199]
	ds_read_b128 v[68:71], v14 offset:10240
	v_mfma_f32_16x16x32_bf16 v[200:203], v[112:115], v[88:91], v[200:203]
	ds_read_b128 v[72:75], v14 offset:12288
	v_mfma_f32_16x16x32_bf16 v[204:207], v[112:115], v[92:95], v[204:207]
	ds_read_b128 v[76:79], v14 offset:14336
	v_mfma_f32_16x16x32_bf16 v[208:211], v[116:119], v[80:83], v[208:211]
	v_mfma_f32_16x16x32_bf16 v[212:215], v[116:119], v[84:87], v[212:215]
	v_mfma_f32_16x16x32_bf16 v[216:219], v[116:119], v[88:91], v[216:219]
	v_mfma_f32_16x16x32_bf16 v[220:223], v[116:119], v[92:95], v[220:223]
	v_mfma_f32_16x16x32_bf16 v[224:227], v[120:123], v[80:83], v[224:227]
	v_mfma_f32_16x16x32_bf16 v[228:231], v[120:123], v[84:87], v[228:231]
	v_mfma_f32_16x16x32_bf16 v[232:235], v[120:123], v[88:91], v[232:235]
	v_mfma_f32_16x16x32_bf16 v[236:239], v[120:123], v[92:95], v[236:239]
	v_mfma_f32_16x16x32_bf16 v[240:243], v[124:127], v[80:83], v[240:243]
	v_mfma_f32_16x16x32_bf16 v[244:247], v[124:127], v[84:87], v[244:247]
	v_mfma_f32_16x16x32_bf16 v[248:251], v[124:127], v[88:91], v[248:251]
	v_mfma_f32_16x16x32_bf16 v[252:255], v[124:127], v[92:95], v[252:255]
	s_waitcnt lgkmcnt(0)
	v_mfma_f32_16x16x32_bf16 v[128:131], v[48:51], v[32:35], v[128:131]
	ds_read_b128 v[80:83], v13 offset:0
	v_mfma_f32_16x16x32_bf16 v[132:135], v[48:51], v[36:39], v[132:135]
	ds_read_b128 v[84:87], v13 offset:2048
	v_mfma_f32_16x16x32_bf16 v[136:139], v[48:51], v[40:43], v[136:139]
	ds_read_b128 v[88:91], v13 offset:4096
	v_mfma_f32_16x16x32_bf16 v[140:143], v[48:51], v[44:47], v[140:143]
	ds_read_b128 v[92:95], v13 offset:6144
	v_mfma_f32_16x16x32_bf16 v[144:147], v[52:55], v[32:35], v[144:147]
	ds_read_b128 v[96:99], v15 offset:0
	v_mfma_f32_16x16x32_bf16 v[148:151], v[52:55], v[36:39], v[148:151]
	ds_read_b128 v[100:103], v15 offset:2048
	v_mfma_f32_16x16x32_bf16 v[152:155], v[52:55], v[40:43], v[152:155]
	ds_read_b128 v[104:107], v15 offset:4096
	v_mfma_f32_16x16x32_bf16 v[156:159], v[52:55], v[44:47], v[156:159]
	ds_read_b128 v[108:111], v15 offset:6144
	v_mfma_f32_16x16x32_bf16 v[160:163], v[56:59], v[32:35], v[160:163]
	ds_read_b128 v[112:115], v15 offset:8192
	v_mfma_f32_16x16x32_bf16 v[164:167], v[56:59], v[36:39], v[164:167]
	ds_read_b128 v[116:119], v15 offset:10240
	v_mfma_f32_16x16x32_bf16 v[168:171], v[56:59], v[40:43], v[168:171]
	ds_read_b128 v[120:123], v15 offset:12288
	v_mfma_f32_16x16x32_bf16 v[172:175], v[56:59], v[44:47], v[172:175]
	ds_read_b128 v[124:127], v15 offset:14336
	v_mfma_f32_16x16x32_bf16 v[176:179], v[60:63], v[32:35], v[176:179]
	v_mfma_f32_16x16x32_bf16 v[180:183], v[60:63], v[36:39], v[180:183]
	v_mfma_f32_16x16x32_bf16 v[184:187], v[60:63], v[40:43], v[184:187]
	v_mfma_f32_16x16x32_bf16 v[188:191], v[60:63], v[44:47], v[188:191]
	v_mfma_f32_16x16x32_bf16 v[192:195], v[64:67], v[32:35], v[192:195]
	v_mfma_f32_16x16x32_bf16 v[196:199], v[64:67], v[36:39], v[196:199]
	v_mfma_f32_16x16x32_bf16 v[200:203], v[64:67], v[40:43], v[200:203]
	v_mfma_f32_16x16x32_bf16 v[204:207], v[64:67], v[44:47], v[204:207]
	v_mfma_f32_16x16x32_bf16 v[208:211], v[68:71], v[32:35], v[208:211]
	v_mfma_f32_16x16x32_bf16 v[212:215], v[68:71], v[36:39], v[212:215]
	v_mfma_f32_16x16x32_bf16 v[216:219], v[68:71], v[40:43], v[216:219]
	v_mfma_f32_16x16x32_bf16 v[220:223], v[68:71], v[44:47], v[220:223]
	v_mfma_f32_16x16x32_bf16 v[224:227], v[72:75], v[32:35], v[224:227]
	v_mfma_f32_16x16x32_bf16 v[228:231], v[72:75], v[36:39], v[228:231]
	v_mfma_f32_16x16x32_bf16 v[232:235], v[72:75], v[40:43], v[232:235]
	v_mfma_f32_16x16x32_bf16 v[236:239], v[72:75], v[44:47], v[236:239]
	v_mfma_f32_16x16x32_bf16 v[240:243], v[76:79], v[32:35], v[240:243]
	v_add_u32_e32 v12, s21, v10
	v_add_u32_e32 v14, s21, v11
	v_xor_b32_e32 v13, 64, v12
	v_xor_b32_e32 v15, 64, v14
	v_mfma_f32_16x16x32_bf16 v[244:247], v[76:79], v[36:39], v[244:247]
	s_add_u32 s21, s21, 0xc000
	s_sub_u32 s23, s21, 0x24000
	s_cmp_ge_u32 s21, 0x24000
	s_cselect_b32 s21, s23, s21
	v_mfma_f32_16x16x32_bf16 v[248:251], v[76:79], v[40:43], v[248:251]
	v_mfma_f32_16x16x32_bf16 v[252:255], v[76:79], v[44:47], v[252:255]
	s_waitcnt lgkmcnt(0)
	v_mfma_f32_16x16x32_bf16 v[128:131], v[96:99], v[80:83], v[128:131]
	v_mfma_f32_16x16x32_bf16 v[132:135], v[96:99], v[84:87], v[132:135]
	v_mfma_f32_16x16x32_bf16 v[136:139], v[96:99], v[88:91], v[136:139]
	v_mfma_f32_16x16x32_bf16 v[140:143], v[96:99], v[92:95], v[140:143]
	v_mfma_f32_16x16x32_bf16 v[144:147], v[100:103], v[80:83], v[144:147]
	v_mfma_f32_16x16x32_bf16 v[148:151], v[100:103], v[84:87], v[148:151]
	v_mfma_f32_16x16x32_bf16 v[152:155], v[100:103], v[88:91], v[152:155]
	v_mfma_f32_16x16x32_bf16 v[156:159], v[100:103], v[92:95], v[156:159]
	s_waitcnt vmcnt(0)
	s_barrier
	v_mfma_f32_16x16x32_bf16 v[160:163], v[104:107], v[80:83], v[160:163]
	ds_read_b128 v[32:35], v12 offset:0
	v_mfma_f32_16x16x32_bf16 v[164:167], v[104:107], v[84:87], v[164:167]
	ds_read_b128 v[36:39], v12 offset:2048
	v_mfma_f32_16x16x32_bf16 v[168:171], v[104:107], v[88:91], v[168:171]
	ds_read_b128 v[40:43], v12 offset:4096
	v_mfma_f32_16x16x32_bf16 v[172:175], v[104:107], v[92:95], v[172:175]
	ds_read_b128 v[44:47], v12 offset:6144
	v_mfma_f32_16x16x32_bf16 v[176:179], v[108:111], v[80:83], v[176:179]
	ds_read_b128 v[48:51], v14 offset:0
	v_mfma_f32_16x16x32_bf16 v[180:183], v[108:111], v[84:87], v[180:183]
	ds_read_b128 v[52:55], v14 offset:2048
	v_mfma_f32_16x16x32_bf16 v[184:187], v[108:111], v[88:91], v[184:187]
	ds_read_b128 v[56:59], v14 offset:4096
	v_mfma_f32_16x16x32_bf16 v[188:191], v[108:111], v[92:95], v[188:191]
	ds_read_b128 v[60:63], v14 offset:6144
	v_mfma_f32_16x16x32_bf16 v[192:195], v[112:115], v[80:83], v[192:195]
	ds_read_b128 v[64:67], v14 offset:8192
	v_mfma_f32_16x16x32_bf16 v[196:199], v[112:115], v[84:87], v[196:199]
	ds_read_b128 v[68:71], v14 offset:10240
	v_mfma_f32_16x16x32_bf16 v[200:203], v[112:115], v[88:91], v[200:203]
	ds_read_b128 v[72:75], v14 offset:12288
	v_mfma_f32_16x16x32_bf16 v[204:207], v[112:115], v[92:95], v[204:207]
	ds_read_b128 v[76:79], v14 offset:14336
	v_mfma_f32_16x16x32_bf16 v[208:211], v[116:119], v[80:83], v[208:211]
	v_mfma_f32_16x16x32_bf16 v[212:215], v[116:119], v[84:87], v[212:215]
	v_mfma_f32_16x16x32_bf16 v[216:219], v[116:119], v[88:91], v[216:219]
	v_mfma_f32_16x16x32_bf16 v[220:223], v[116:119], v[92:95], v[220:223]
	v_mfma_f32_16x16x32_bf16 v[224:227], v[120:123], v[80:83], v[224:227]
	v_mfma_f32_16x16x32_bf16 v[228:231], v[120:123], v[84:87], v[228:231]
	v_mfma_f32_16x16x32_bf16 v[232:235], v[120:123], v[88:91], v[232:235]
	v_mfma_f32_16x16x32_bf16 v[236:239], v[120:123], v[92:95], v[236:239]
	v_mfma_f32_16x16x32_bf16 v[240:243], v[124:127], v[80:83], v[240:243]
	v_mfma_f32_16x16x32_bf16 v[244:247], v[124:127], v[84:87], v[244:247]
	v_mfma_f32_16x16x32_bf16 v[248:251], v[124:127], v[88:91], v[248:251]
	v_mfma_f32_16x16x32_bf16 v[252:255], v[124:127], v[92:95], v[252:255]
	s_waitcnt lgkmcnt(0)
	v_mfma_f32_16x16x32_bf16 v[128:131], v[48:51], v[32:35], v[128:131]
	ds_read_b128 v[80:83], v13 offset:0
	v_mfma_f32_16x16x32_bf16 v[132:135], v[48:51], v[36:39], v[132:135]
	ds_read_b128 v[84:87], v13 offset:2048
	v_mfma_f32_16x16x32_bf16 v[136:139], v[48:51], v[40:43], v[136:139]
	ds_read_b128 v[88:91], v13 offset:4096
	v_mfma_f32_16x16x32_bf16 v[140:143], v[48:51], v[44:47], v[140:143]
	ds_read_b128 v[92:95], v13 offset:6144
	v_mfma_f32_16x16x32_bf16 v[144:147], v[52:55], v[32:35], v[144:147]
	ds_read_b128 v[96:99], v15 offset:0
	v_mfma_f32_16x16x32_bf16 v[148:151], v[52:55], v[36:39], v[148:151]
	ds_read_b128 v[100:103], v15 offset:2048
	v_mfma_f32_16x16x32_bf16 v[152:155], v[52:55], v[40:43], v[152:155]
	ds_read_b128 v[104:107], v15 offset:4096
	v_mfma_f32_16x16x32_bf16 v[156:159], v[52:55], v[44:47], v[156:159]
	ds_read_b128 v[108:111], v15 offset:6144
	v_mfma_f32_16x16x32_bf16 v[160:163], v[56:59], v[32:35], v[160:163]
	ds_read_b128 v[112:115], v15 offset:8192
	v_mfma_f32_16x16x32_bf16 v[164:167], v[56:59], v[36:39], v[164:167]
	ds_read_b128 v[116:119], v15 offset:10240
	v_mfma_f32_16x16x32_bf16 v[168:171], v[56:59], v[40:43], v[168:171]
	ds_read_b128 v[120:123], v15 offset:12288
	v_mfma_f32_16x16x32_bf16 v[172:175], v[56:59], v[44:47], v[172:175]
	ds_read_b128 v[124:127], v15 offset:14336
	v_mfma_f32_16x16x32_bf16 v[176:179], v[60:63], v[32:35], v[176:179]
	v_mfma_f32_16x16x32_bf16 v[180:183], v[60:63], v[36:39], v[180:183]
	v_mfma_f32_16x16x32_bf16 v[184:187], v[60:63], v[40:43], v[184:187]
	v_mfma_f32_16x16x32_bf16 v[188:191], v[60:63], v[44:47], v[188:191]
	v_mfma_f32_16x16x32_bf16 v[192:195], v[64:67], v[32:35], v[192:195]
	v_mfma_f32_16x16x32_bf16 v[196:199], v[64:67], v[36:39], v[196:199]
	v_mfma_f32_16x16x32_bf16 v[200:203], v[64:67], v[40:43], v[200:203]
	v_mfma_f32_16x16x32_bf16 v[204:207], v[64:67], v[44:47], v[204:207]
	v_mfma_f32_16x16x32_bf16 v[208:211], v[68:71], v[32:35], v[208:211]
	v_mfma_f32_16x16x32_bf16 v[212:215], v[68:71], v[36:39], v[212:215]
	v_mfma_f32_16x16x32_bf16 v[216:219], v[68:71], v[40:43], v[216:219]
	v_mfma_f32_16x16x32_bf16 v[220:223], v[68:71], v[44:47], v[220:223]
	v_mfma_f32_16x16x32_bf16 v[224:227], v[72:75], v[32:35], v[224:227]
	v_mfma_f32_16x16x32_bf16 v[228:231], v[72:75], v[36:39], v[228:231]
	v_mfma_f32_16x16x32_bf16 v[232:235], v[72:75], v[40:43], v[232:235]
	v_mfma_f32_16x16x32_bf16 v[236:239], v[72:75], v[44:47], v[236:239]
	v_mfma_f32_16x16x32_bf16 v[240:243], v[76:79], v[32:35], v[240:243]
	v_mfma_f32_16x16x32_bf16 v[244:247], v[76:79], v[36:39], v[244:247]
	v_mfma_f32_16x16x32_bf16 v[248:251], v[76:79], v[40:43], v[248:251]
	v_mfma_f32_16x16x32_bf16 v[252:255], v[76:79], v[44:47], v[252:255]
	s_waitcnt lgkmcnt(0)
	v_mfma_f32_16x16x32_bf16 v[128:131], v[96:99], v[80:83], v[128:131]
	v_mfma_f32_16x16x32_bf16 v[132:135], v[96:99], v[84:87], v[132:135]
	global_load_dwordx4 v[32:35], v21, s[8:9] offset:0
	v_mfma_f32_16x16x32_bf16 v[136:139], v[96:99], v[88:91], v[136:139]
	v_mfma_f32_16x16x32_bf16 v[140:143], v[96:99], v[92:95], v[140:143]
	global_load_dwordx4 v[36:39], v21, s[8:9] offset:16
	v_mfma_f32_16x16x32_bf16 v[144:147], v[100:103], v[80:83], v[144:147]
	v_mfma_f32_16x16x32_bf16 v[148:151], v[100:103], v[84:87], v[148:151]
	global_load_dwordx4 v[40:43], v21, s[8:9] offset:32
	v_mfma_f32_16x16x32_bf16 v[152:155], v[100:103], v[88:91], v[152:155]
	v_mfma_f32_16x16x32_bf16 v[156:159], v[100:103], v[92:95], v[156:159]
	global_load_dwordx4 v[44:47], v21, s[8:9] offset:48
	v_mfma_f32_16x16x32_bf16 v[160:163], v[104:107], v[80:83], v[160:163]
	v_mfma_f32_16x16x32_bf16 v[164:167], v[104:107], v[84:87], v[164:167]
	global_load_dwordx4 v[48:51], v21, s[8:9] offset:1024
	v_mfma_f32_16x16x32_bf16 v[168:171], v[104:107], v[88:91], v[168:171]
	v_mfma_f32_16x16x32_bf16 v[172:175], v[104:107], v[92:95], v[172:175]
	global_load_dwordx4 v[52:55], v21, s[8:9] offset:1040
	v_mfma_f32_16x16x32_bf16 v[176:179], v[108:111], v[80:83], v[176:179]
	v_mfma_f32_16x16x32_bf16 v[180:183], v[108:111], v[84:87], v[180:183]
	global_load_dwordx4 v[56:59], v21, s[8:9] offset:1056
	v_mfma_f32_16x16x32_bf16 v[184:187], v[108:111], v[88:91], v[184:187]
	v_mfma_f32_16x16x32_bf16 v[188:191], v[108:111], v[92:95], v[188:191]
	global_load_dwordx4 v[60:63], v21, s[8:9] offset:1072
	v_mfma_f32_16x16x32_bf16 v[192:195], v[112:115], v[80:83], v[192:195]
	v_mfma_f32_16x16x32_bf16 v[196:199], v[112:115], v[84:87], v[196:199]
	global_load_dwordx4 v[64:67], v21, s[8:9] offset:2048
	v_mfma_f32_16x16x32_bf16 v[200:203], v[112:115], v[88:91], v[200:203]
	v_mfma_f32_16x16x32_bf16 v[204:207], v[112:115], v[92:95], v[204:207]
	global_load_dwordx4 v[68:71], v21, s[8:9] offset:2064
	v_mfma_f32_16x16x32_bf16 v[208:211], v[116:119], v[80:83], v[208:211]
	v_mfma_f32_16x16x32_bf16 v[212:215], v[116:119], v[84:87], v[212:215]
	global_load_dwordx4 v[72:75], v21, s[8:9] offset:2080
	v_mfma_f32_16x16x32_bf16 v[216:219], v[116:119], v[88:91], v[216:219]
	v_mfma_f32_16x16x32_bf16 v[220:223], v[116:119], v[92:95], v[220:223]
	global_load_dwordx4 v[76:79], v21, s[8:9] offset:2096
	v_mfma_f32_16x16x32_bf16 v[224:227], v[120:123], v[80:83], v[224:227]
	v_mfma_f32_16x16x32_bf16 v[228:231], v[120:123], v[84:87], v[228:231]
	v_mfma_f32_16x16x32_bf16 v[232:235], v[120:123], v[88:91], v[232:235]
	v_mfma_f32_16x16x32_bf16 v[236:239], v[120:123], v[92:95], v[236:239]
	v_mfma_f32_16x16x32_bf16 v[240:243], v[124:127], v[80:83], v[240:243]
	v_mfma_f32_16x16x32_bf16 v[244:247], v[124:127], v[84:87], v[244:247]
	v_mfma_f32_16x16x32_bf16 v[248:251], v[124:127], v[88:91], v[248:251]
	v_mfma_f32_16x16x32_bf16 v[252:255], v[124:127], v[92:95], v[252:255]
	global_load_dwordx4 v[80:83], v21, s[8:9] offset:3072
	global_load_dwordx4 v[84:87], v21, s[8:9] offset:3088
	global_load_dwordx4 v[88:91], v21, s[8:9] offset:3104
	global_load_dwordx4 v[92:95], v21, s[8:9] offset:3120
	v_mov_b32_e32 v31, 0x358637bd
	s_waitcnt vmcnt(0)
	v_add_f32_e32 v32, v32, v33
	v_add_f32_e32 v34, v34, v35
	v_add_f32_e32 v36, v36, v37
	v_add_f32_e32 v38, v38, v39
	v_add_f32_e32 v40, v40, v41
	v_add_f32_e32 v42, v42, v43
	v_add_f32_e32 v44, v44, v45
	v_add_f32_e32 v46, v46, v47
	v_add_f32_e32 v32, v32, v34
	v_add_f32_e32 v36, v36, v38
	v_add_f32_e32 v40, v40, v42
	v_add_f32_e32 v44, v44, v46
	v_add_f32_e32 v32, v32, v36
	v_add_f32_e32 v40, v40, v44
	v_add_f32_e32 v32, v32, v40
	v_add_f32_e32 v48, v48, v49
	v_add_f32_e32 v50, v50, v51
	v_add_f32_e32 v52, v52, v53
	v_add_f32_e32 v54, v54, v55
	v_add_f32_e32 v56, v56, v57
	v_add_f32_e32 v58, v58, v59
	v_add_f32_e32 v60, v60, v61
	v_add_f32_e32 v62, v62, v63
	v_add_f32_e32 v48, v48, v50
	v_add_f32_e32 v52, v52, v54
	v_add_f32_e32 v56, v56, v58
	v_add_f32_e32 v60, v60, v62
	v_add_f32_e32 v48, v48, v52
	v_add_f32_e32 v56, v56, v60
	v_add_f32_e32 v48, v48, v56
	v_add_f32_e32 v64, v64, v65
	v_add_f32_e32 v66, v66, v67
	v_add_f32_e32 v68, v68, v69
	v_add_f32_e32 v70, v70, v71
	v_add_f32_e32 v72, v72, v73
	v_add_f32_e32 v74, v74, v75
	v_add_f32_e32 v76, v76, v77
	v_add_f32_e32 v78, v78, v79
	v_add_f32_e32 v64, v64, v66
	v_add_f32_e32 v68, v68, v70
	v_add_f32_e32 v72, v72, v74
	v_add_f32_e32 v76, v76, v78
	v_add_f32_e32 v64, v64, v68
	v_add_f32_e32 v72, v72, v76
	v_add_f32_e32 v64, v64, v72
	v_add_f32_e32 v80, v80, v81
	v_add_f32_e32 v82, v82, v83
	v_add_f32_e32 v84, v84, v85
	v_add_f32_e32 v86, v86, v87
	v_add_f32_e32 v88, v88, v89
	v_add_f32_e32 v90, v90, v91
	v_add_f32_e32 v92, v92, v93
	v_add_f32_e32 v94, v94, v95
	v_add_f32_e32 v80, v80, v82
	v_add_f32_e32 v84, v84, v86
	v_add_f32_e32 v88, v88, v90
	v_add_f32_e32 v92, v92, v94
	v_add_f32_e32 v80, v80, v84
	v_add_f32_e32 v88, v88, v92
	v_add_f32_e32 v80, v80, v88
	v_fmamk_f32 v20, v32, 0x3aaaaaab, v31
	v_fmamk_f32 v22, v48, 0x3aaaaaab, v31
	v_fmamk_f32 v24, v64, 0x3aaaaaab, v31
	v_fmamk_f32 v26, v80, 0x3aaaaaab, v31
	v_rsq_f32_e32 v20, v20
	v_rsq_f32_e32 v22, v22
	v_rsq_f32_e32 v24, v24
	v_rsq_f32_e32 v26, v26
	s_nop 0
	v_pk_mul_f32 v[128:129], v[128:129], v[20:21] op_sel_hi:[1,0]
	v_pk_mul_f32 v[130:131], v[130:131], v[20:21] op_sel_hi:[1,0]
	v_pk_mul_f32 v[144:145], v[144:145], v[20:21] op_sel_hi:[1,0]
	v_pk_mul_f32 v[146:147], v[146:147], v[20:21] op_sel_hi:[1,0]
	v_pk_mul_f32 v[32:33], v[128:129], s[26:27]
	v_pk_mul_f32 v[34:35], v[130:131], s[26:27]
	v_pk_mul_f32 v[36:37], v[144:145], s[26:27]
	v_pk_mul_f32 v[38:39], v[146:147], s[26:27]
	v_pk_fma_f32 v[32:33], v[128:129], v[32:33], s[28:29] neg_lo:[1,0,0] neg_hi:[1,0,0]
	v_pk_fma_f32 v[34:35], v[130:131], v[34:35], s[28:29] neg_lo:[1,0,0] neg_hi:[1,0,0]
	v_pk_fma_f32 v[36:37], v[144:145], v[36:37], s[28:29] neg_lo:[1,0,0] neg_hi:[1,0,0]
	v_pk_fma_f32 v[38:39], v[146:147], v[38:39], s[28:29] neg_lo:[1,0,0] neg_hi:[1,0,0]
	v_pk_mul_f32 v[32:33], v[128:129], v[32:33]
	v_pk_mul_f32 v[34:35], v[130:131], v[34:35]
	v_pk_mul_f32 v[36:37], v[144:145], v[36:37]
	v_pk_mul_f32 v[38:39], v[146:147], v[38:39]
	v_exp_f32_e32 v32, v32
	v_exp_f32_e32 v33, v33
	v_exp_f32_e32 v34, v34
	v_exp_f32_e32 v35, v35
	v_exp_f32_e32 v36, v36
	v_exp_f32_e32 v37, v37
	v_exp_f32_e32 v38, v38
	v_exp_f32_e32 v39, v39
	v_pk_add_f32 v[32:33], v[32:33], s[30:31]
	v_pk_add_f32 v[34:35], v[34:35], s[30:31]
	v_pk_add_f32 v[36:37], v[36:37], s[30:31]
	v_pk_add_f32 v[38:39], v[38:39], s[30:31]
	v_rcp_f32_e32 v32, v32
	v_rcp_f32_e32 v33, v33
	v_rcp_f32_e32 v34, v34
	v_rcp_f32_e32 v35, v35
	v_rcp_f32_e32 v36, v36
	v_rcp_f32_e32 v37, v37
	v_rcp_f32_e32 v38, v38
	v_rcp_f32_e32 v39, v39
	s_nop 0
	v_pk_mul_f32 v[128:129], v[128:129], v[32:33]
	v_pk_mul_f32 v[130:131], v[130:131], v[34:35]
	v_pk_mul_f32 v[144:145], v[144:145], v[36:37]
	v_pk_mul_f32 v[146:147], v[146:147], v[38:39]
	v_cvt_pk_bf16_f32 v64, v128, v129
	v_cvt_pk_bf16_f32 v65, v130, v131
	v_cvt_pk_bf16_f32 v66, v144, v145
	v_cvt_pk_bf16_f32 v67, v146, v147
	global_store_dwordx2 v16, v[64:65], s[10:11]
	global_store_dwordx2 v16, v[66:67], s[10:11] offset:32
	v_pk_mul_f32 v[160:161], v[160:161], v[20:21] op_sel_hi:[1,0]
	v_pk_mul_f32 v[162:163], v[162:163], v[20:21] op_sel_hi:[1,0]
	v_pk_mul_f32 v[176:177], v[176:177], v[20:21] op_sel_hi:[1,0]
	v_pk_mul_f32 v[178:179], v[178:179], v[20:21] op_sel_hi:[1,0]
	v_pk_mul_f32 v[48:49], v[160:161], s[26:27]
	v_pk_mul_f32 v[50:51], v[162:163], s[26:27]
	v_pk_mul_f32 v[52:53], v[176:177], s[26:27]
	v_pk_mul_f32 v[54:55], v[178:179], s[26:27]
	v_pk_fma_f32 v[48:49], v[160:161], v[48:49], s[28:29] neg_lo:[1,0,0] neg_hi:[1,0,0]
	v_pk_fma_f32 v[50:51], v[162:163], v[50:51], s[28:29] neg_lo:[1,0,0] neg_hi:[1,0,0]
	v_pk_fma_f32 v[52:53], v[176:177], v[52:53], s[28:29] neg_lo:[1,0,0] neg_hi:[1,0,0]
	v_pk_fma_f32 v[54:55], v[178:179], v[54:55], s[28:29] neg_lo:[1,0,0] neg_hi:[1,0,0]
	v_pk_mul_f32 v[48:49], v[160:161], v[48:49]
	v_pk_mul_f32 v[50:51], v[162:163], v[50:51]
	v_pk_mul_f32 v[52:53], v[176:177], v[52:53]
	v_pk_mul_f32 v[54:55], v[178:179], v[54:55]
	v_exp_f32_e32 v48, v48
	v_exp_f32_e32 v49, v49
	v_exp_f32_e32 v50, v50
	v_exp_f32_e32 v51, v51
	v_exp_f32_e32 v52, v52
	v_exp_f32_e32 v53, v53
	v_exp_f32_e32 v54, v54
	v_exp_f32_e32 v55, v55
	v_pk_add_f32 v[48:49], v[48:49], s[30:31]
	v_pk_add_f32 v[50:51], v[50:51], s[30:31]
	v_pk_add_f32 v[52:53], v[52:53], s[30:31]
	v_pk_add_f32 v[54:55], v[54:55], s[30:31]
	v_rcp_f32_e32 v48, v48
	v_rcp_f32_e32 v49, v49
	v_rcp_f32_e32 v50, v50
	v_rcp_f32_e32 v51, v51
	v_rcp_f32_e32 v52, v52
	v_rcp_f32_e32 v53, v53
	v_rcp_f32_e32 v54, v54
	v_rcp_f32_e32 v55, v55
	s_nop 0
	v_pk_mul_f32 v[160:161], v[160:161], v[48:49]
	v_pk_mul_f32 v[162:163], v[162:163], v[50:51]
	v_pk_mul_f32 v[176:177], v[176:177], v[52:53]
	v_pk_mul_f32 v[178:179], v[178:179], v[54:55]
	v_cvt_pk_bf16_f32 v68, v160, v161
	v_cvt_pk_bf16_f32 v69, v162, v163
	v_cvt_pk_bf16_f32 v70, v176, v177
	v_cvt_pk_bf16_f32 v71, v178, v179
	global_store_dwordx2 v16, v[68:69], s[10:11] offset:64
	global_store_dwordx2 v16, v[70:71], s[10:11] offset:96
	v_pk_mul_f32 v[192:193], v[192:193], v[20:21] op_sel_hi:[1,0]
	v_pk_mul_f32 v[194:195], v[194:195], v[20:21] op_sel_hi:[1,0]
	v_pk_mul_f32 v[208:209], v[208:209], v[20:21] op_sel_hi:[1,0]
	v_pk_mul_f32 v[210:211], v[210:211], v[20:21] op_sel_hi:[1,0]
	v_pk_mul_f32 v[32:33], v[192:193], s[26:27]
	v_pk_mul_f32 v[34:35], v[194:195], s[26:27]
	v_pk_mul_f32 v[36:37], v[208:209], s[26:27]
	v_pk_mul_f32 v[38:39], v[210:211], s[26:27]
	v_pk_fma_f32 v[32:33], v[192:193], v[32:33], s[28:29] neg_lo:[1,0,0] neg_hi:[1,0,0]
	v_pk_fma_f32 v[34:35], v[194:195], v[34:35], s[28:29] neg_lo:[1,0,0] neg_hi:[1,0,0]
	v_pk_fma_f32 v[36:37], v[208:209], v[36:37], s[28:29] neg_lo:[1,0,0] neg_hi:[1,0,0]
	v_pk_fma_f32 v[38:39], v[210:211], v[38:39], s[28:29] neg_lo:[1,0,0] neg_hi:[1,0,0]
	v_pk_mul_f32 v[32:33], v[192:193], v[32:33]
	v_pk_mul_f32 v[34:35], v[194:195], v[34:35]
	v_pk_mul_f32 v[36:37], v[208:209], v[36:37]
	v_pk_mul_f32 v[38:39], v[210:211], v[38:39]
	v_exp_f32_e32 v32, v32
	v_exp_f32_e32 v33, v33
	v_exp_f32_e32 v34, v34
	v_exp_f32_e32 v35, v35
	v_exp_f32_e32 v36, v36
	v_exp_f32_e32 v37, v37
	v_exp_f32_e32 v38, v38
	v_exp_f32_e32 v39, v39
	v_pk_add_f32 v[32:33], v[32:33], s[30:31]
	v_pk_add_f32 v[34:35], v[34:35], s[30:31]
	v_pk_add_f32 v[36:37], v[36:37], s[30:31]
	v_pk_add_f32 v[38:39], v[38:39], s[30:31]
	v_rcp_f32_e32 v32, v32
	v_rcp_f32_e32 v33, v33
	v_rcp_f32_e32 v34, v34
	v_rcp_f32_e32 v35, v35
	v_rcp_f32_e32 v36, v36
	v_rcp_f32_e32 v37, v37
	v_rcp_f32_e32 v38, v38
	v_rcp_f32_e32 v39, v39
	s_nop 0
	v_pk_mul_f32 v[192:193], v[192:193], v[32:33]
	v_pk_mul_f32 v[194:195], v[194:195], v[34:35]
	v_pk_mul_f32 v[208:209], v[208:209], v[36:37]
	v_pk_mul_f32 v[210:211], v[210:211], v[38:39]
	v_cvt_pk_bf16_f32 v64, v192, v193
	v_cvt_pk_bf16_f32 v65, v194, v195
	v_cvt_pk_bf16_f32 v66, v208, v209
	v_cvt_pk_bf16_f32 v67, v210, v211
	global_store_dwordx2 v16, v[64:65], s[10:11] offset:128
	global_store_dwordx2 v16, v[66:67], s[10:11] offset:160
	v_pk_mul_f32 v[224:225], v[224:225], v[20:21] op_sel_hi:[1,0]
	v_pk_mul_f32 v[226:227], v[226:227], v[20:21] op_sel_hi:[1,0]
	v_pk_mul_f32 v[240:241], v[240:241], v[20:21] op_sel_hi:[1,0]
	v_pk_mul_f32 v[242:243], v[242:243], v[20:21] op_sel_hi:[1,0]
	v_pk_mul_f32 v[48:49], v[224:225], s[26:27]
	v_pk_mul_f32 v[50:51], v[226:227], s[26:27]
	v_pk_mul_f32 v[52:53], v[240:241], s[26:27]
	v_pk_mul_f32 v[54:55], v[242:243], s[26:27]
	v_pk_fma_f32 v[48:49], v[224:225], v[48:49], s[28:29] neg_lo:[1,0,0] neg_hi:[1,0,0]
	v_pk_fma_f32 v[50:51], v[226:227], v[50:51], s[28:29] neg_lo:[1,0,0] neg_hi:[1,0,0]
	v_pk_fma_f32 v[52:53], v[240:241], v[52:53], s[28:29] neg_lo:[1,0,0] neg_hi:[1,0,0]
	v_pk_fma_f32 v[54:55], v[242:243], v[54:55], s[28:29] neg_lo:[1,0,0] neg_hi:[1,0,0]
	v_pk_mul_f32 v[48:49], v[224:225], v[48:49]
	v_pk_mul_f32 v[50:51], v[226:227], v[50:51]
	v_pk_mul_f32 v[52:53], v[240:241], v[52:53]
	v_pk_mul_f32 v[54:55], v[242:243], v[54:55]
	v_exp_f32_e32 v48, v48
	v_exp_f32_e32 v49, v49
	v_exp_f32_e32 v50, v50
	v_exp_f32_e32 v51, v51
	v_exp_f32_e32 v52, v52
	v_exp_f32_e32 v53, v53
	v_exp_f32_e32 v54, v54
	v_exp_f32_e32 v55, v55
	v_pk_add_f32 v[48:49], v[48:49], s[30:31]
	v_pk_add_f32 v[50:51], v[50:51], s[30:31]
	v_pk_add_f32 v[52:53], v[52:53], s[30:31]
	v_pk_add_f32 v[54:55], v[54:55], s[30:31]
	v_rcp_f32_e32 v48, v48
	v_rcp_f32_e32 v49, v49
	v_rcp_f32_e32 v50, v50
	v_rcp_f32_e32 v51, v51
	v_rcp_f32_e32 v52, v52
	v_rcp_f32_e32 v53, v53
	v_rcp_f32_e32 v54, v54
	v_rcp_f32_e32 v55, v55
	s_nop 0
	v_pk_mul_f32 v[224:225], v[224:225], v[48:49]
	v_pk_mul_f32 v[226:227], v[226:227], v[50:51]
	v_pk_mul_f32 v[240:241], v[240:241], v[52:53]
	v_pk_mul_f32 v[242:243], v[242:243], v[54:55]
	v_cvt_pk_bf16_f32 v68, v224, v225
	v_cvt_pk_bf16_f32 v69, v226, v227
	v_cvt_pk_bf16_f32 v70, v240, v241
	v_cvt_pk_bf16_f32 v71, v242, v243
	global_store_dwordx2 v16, v[68:69], s[10:11] offset:192
	global_store_dwordx2 v16, v[70:71], s[10:11] offset:224
	v_pk_mul_f32 v[132:133], v[132:133], v[22:23] op_sel_hi:[1,0]
	v_pk_mul_f32 v[134:135], v[134:135], v[22:23] op_sel_hi:[1,0]
	v_pk_mul_f32 v[148:149], v[148:149], v[22:23] op_sel_hi:[1,0]
	v_pk_mul_f32 v[150:151], v[150:151], v[22:23] op_sel_hi:[1,0]
	v_pk_mul_f32 v[32:33], v[132:133], s[26:27]
	v_pk_mul_f32 v[34:35], v[134:135], s[26:27]
	v_pk_mul_f32 v[36:37], v[148:149], s[26:27]
	v_pk_mul_f32 v[38:39], v[150:151], s[26:27]
	v_pk_fma_f32 v[32:33], v[132:133], v[32:33], s[28:29] neg_lo:[1,0,0] neg_hi:[1,0,0]
	v_pk_fma_f32 v[34:35], v[134:135], v[34:35], s[28:29] neg_lo:[1,0,0] neg_hi:[1,0,0]
	v_pk_fma_f32 v[36:37], v[148:149], v[36:37], s[28:29] neg_lo:[1,0,0] neg_hi:[1,0,0]
	v_pk_fma_f32 v[38:39], v[150:151], v[38:39], s[28:29] neg_lo:[1,0,0] neg_hi:[1,0,0]
	v_pk_mul_f32 v[32:33], v[132:133], v[32:33]
	v_pk_mul_f32 v[34:35], v[134:135], v[34:35]
	v_pk_mul_f32 v[36:37], v[148:149], v[36:37]
	v_pk_mul_f32 v[38:39], v[150:151], v[38:39]
	v_exp_f32_e32 v32, v32
	v_exp_f32_e32 v33, v33
	v_exp_f32_e32 v34, v34
	v_exp_f32_e32 v35, v35
	v_exp_f32_e32 v36, v36
	v_exp_f32_e32 v37, v37
	v_exp_f32_e32 v38, v38
	v_exp_f32_e32 v39, v39
	v_pk_add_f32 v[32:33], v[32:33], s[30:31]
	v_pk_add_f32 v[34:35], v[34:35], s[30:31]
	v_pk_add_f32 v[36:37], v[36:37], s[30:31]
	v_pk_add_f32 v[38:39], v[38:39], s[30:31]
	v_rcp_f32_e32 v32, v32
	v_rcp_f32_e32 v33, v33
	v_rcp_f32_e32 v34, v34
	v_rcp_f32_e32 v35, v35
	v_rcp_f32_e32 v36, v36
	v_rcp_f32_e32 v37, v37
	v_rcp_f32_e32 v38, v38
	v_rcp_f32_e32 v39, v39
	s_nop 0
	v_pk_mul_f32 v[132:133], v[132:133], v[32:33]
	v_pk_mul_f32 v[134:135], v[134:135], v[34:35]
	v_pk_mul_f32 v[148:149], v[148:149], v[36:37]
	v_pk_mul_f32 v[150:151], v[150:151], v[38:39]
	v_cvt_pk_bf16_f32 v64, v132, v133
	v_cvt_pk_bf16_f32 v65, v134, v135
	v_cvt_pk_bf16_f32 v66, v148, v149
	v_cvt_pk_bf16_f32 v67, v150, v151
	global_store_dwordx2 v17, v[64:65], s[10:11]
	global_store_dwordx2 v17, v[66:67], s[10:11] offset:32
	v_pk_mul_f32 v[164:165], v[164:165], v[22:23] op_sel_hi:[1,0]
	v_pk_mul_f32 v[166:167], v[166:167], v[22:23] op_sel_hi:[1,0]
	v_pk_mul_f32 v[180:181], v[180:181], v[22:23] op_sel_hi:[1,0]
	v_pk_mul_f32 v[182:183], v[182:183], v[22:23] op_sel_hi:[1,0]
	v_pk_mul_f32 v[48:49], v[164:165], s[26:27]
	v_pk_mul_f32 v[50:51], v[166:167], s[26:27]
	v_pk_mul_f32 v[52:53], v[180:181], s[26:27]
	v_pk_mul_f32 v[54:55], v[182:183], s[26:27]
	v_pk_fma_f32 v[48:49], v[164:165], v[48:49], s[28:29] neg_lo:[1,0,0] neg_hi:[1,0,0]
	v_pk_fma_f32 v[50:51], v[166:167], v[50:51], s[28:29] neg_lo:[1,0,0] neg_hi:[1,0,0]
	v_pk_fma_f32 v[52:53], v[180:181], v[52:53], s[28:29] neg_lo:[1,0,0] neg_hi:[1,0,0]
	v_pk_fma_f32 v[54:55], v[182:183], v[54:55], s[28:29] neg_lo:[1,0,0] neg_hi:[1,0,0]
	v_pk_mul_f32 v[48:49], v[164:165], v[48:49]
	v_pk_mul_f32 v[50:51], v[166:167], v[50:51]
	v_pk_mul_f32 v[52:53], v[180:181], v[52:53]
	v_pk_mul_f32 v[54:55], v[182:183], v[54:55]
	v_exp_f32_e32 v48, v48
	v_exp_f32_e32 v49, v49
	v_exp_f32_e32 v50, v50
	v_exp_f32_e32 v51, v51
	v_exp_f32_e32 v52, v52
	v_exp_f32_e32 v53, v53
	v_exp_f32_e32 v54, v54
	v_exp_f32_e32 v55, v55
	v_pk_add_f32 v[48:49], v[48:49], s[30:31]
	v_pk_add_f32 v[50:51], v[50:51], s[30:31]
	v_pk_add_f32 v[52:53], v[52:53], s[30:31]
	v_pk_add_f32 v[54:55], v[54:55], s[30:31]
	v_rcp_f32_e32 v48, v48
	v_rcp_f32_e32 v49, v49
	v_rcp_f32_e32 v50, v50
	v_rcp_f32_e32 v51, v51
	v_rcp_f32_e32 v52, v52
	v_rcp_f32_e32 v53, v53
	v_rcp_f32_e32 v54, v54
	v_rcp_f32_e32 v55, v55
	s_nop 0
	v_pk_mul_f32 v[164:165], v[164:165], v[48:49]
	v_pk_mul_f32 v[166:167], v[166:167], v[50:51]
	v_pk_mul_f32 v[180:181], v[180:181], v[52:53]
	v_pk_mul_f32 v[182:183], v[182:183], v[54:55]
	v_cvt_pk_bf16_f32 v68, v164, v165
	v_cvt_pk_bf16_f32 v69, v166, v167
	v_cvt_pk_bf16_f32 v70, v180, v181
	v_cvt_pk_bf16_f32 v71, v182, v183
	global_store_dwordx2 v17, v[68:69], s[10:11] offset:64
	global_store_dwordx2 v17, v[70:71], s[10:11] offset:96
	v_pk_mul_f32 v[196:197], v[196:197], v[22:23] op_sel_hi:[1,0]
	v_pk_mul_f32 v[198:199], v[198:199], v[22:23] op_sel_hi:[1,0]
	v_pk_mul_f32 v[212:213], v[212:213], v[22:23] op_sel_hi:[1,0]
	v_pk_mul_f32 v[214:215], v[214:215], v[22:23] op_sel_hi:[1,0]
	v_pk_mul_f32 v[32:33], v[196:197], s[26:27]
	v_pk_mul_f32 v[34:35], v[198:199], s[26:27]
	v_pk_mul_f32 v[36:37], v[212:213], s[26:27]
	v_pk_mul_f32 v[38:39], v[214:215], s[26:27]
	v_pk_fma_f32 v[32:33], v[196:197], v[32:33], s[28:29] neg_lo:[1,0,0] neg_hi:[1,0,0]
	v_pk_fma_f32 v[34:35], v[198:199], v[34:35], s[28:29] neg_lo:[1,0,0] neg_hi:[1,0,0]
	v_pk_fma_f32 v[36:37], v[212:213], v[36:37], s[28:29] neg_lo:[1,0,0] neg_hi:[1,0,0]
	v_pk_fma_f32 v[38:39], v[214:215], v[38:39], s[28:29] neg_lo:[1,0,0] neg_hi:[1,0,0]
	v_pk_mul_f32 v[32:33], v[196:197], v[32:33]
	v_pk_mul_f32 v[34:35], v[198:199], v[34:35]
	v_pk_mul_f32 v[36:37], v[212:213], v[36:37]
	v_pk_mul_f32 v[38:39], v[214:215], v[38:39]
	v_exp_f32_e32 v32, v32
	v_exp_f32_e32 v33, v33
	v_exp_f32_e32 v34, v34
	v_exp_f32_e32 v35, v35
	v_exp_f32_e32 v36, v36
	v_exp_f32_e32 v37, v37
	v_exp_f32_e32 v38, v38
	v_exp_f32_e32 v39, v39
	v_pk_add_f32 v[32:33], v[32:33], s[30:31]
	v_pk_add_f32 v[34:35], v[34:35], s[30:31]
	v_pk_add_f32 v[36:37], v[36:37], s[30:31]
	v_pk_add_f32 v[38:39], v[38:39], s[30:31]
	v_rcp_f32_e32 v32, v32
	v_rcp_f32_e32 v33, v33
	v_rcp_f32_e32 v34, v34
	v_rcp_f32_e32 v35, v35
	v_rcp_f32_e32 v36, v36
	v_rcp_f32_e32 v37, v37
	v_rcp_f32_e32 v38, v38
	v_rcp_f32_e32 v39, v39
	s_nop 0
	v_pk_mul_f32 v[196:197], v[196:197], v[32:33]
	v_pk_mul_f32 v[198:199], v[198:199], v[34:35]
	v_pk_mul_f32 v[212:213], v[212:213], v[36:37]
	v_pk_mul_f32 v[214:215], v[214:215], v[38:39]
	v_cvt_pk_bf16_f32 v64, v196, v197
	v_cvt_pk_bf16_f32 v65, v198, v199
	v_cvt_pk_bf16_f32 v66, v212, v213
	v_cvt_pk_bf16_f32 v67, v214, v215
	global_store_dwordx2 v17, v[64:65], s[10:11] offset:128
	global_store_dwordx2 v17, v[66:67], s[10:11] offset:160
	v_pk_mul_f32 v[228:229], v[228:229], v[22:23] op_sel_hi:[1,0]
	v_pk_mul_f32 v[230:231], v[230:231], v[22:23] op_sel_hi:[1,0]
	v_pk_mul_f32 v[244:245], v[244:245], v[22:23] op_sel_hi:[1,0]
	v_pk_mul_f32 v[246:247], v[246:247], v[22:23] op_sel_hi:[1,0]
	v_pk_mul_f32 v[48:49], v[228:229], s[26:27]
	v_pk_mul_f32 v[50:51], v[230:231], s[26:27]
	v_pk_mul_f32 v[52:53], v[244:245], s[26:27]
	v_pk_mul_f32 v[54:55], v[246:247], s[26:27]
	v_pk_fma_f32 v[48:49], v[228:229], v[48:49], s[28:29] neg_lo:[1,0,0] neg_hi:[1,0,0]
	v_pk_fma_f32 v[50:51], v[230:231], v[50:51], s[28:29] neg_lo:[1,0,0] neg_hi:[1,0,0]
	v_pk_fma_f32 v[52:53], v[244:245], v[52:53], s[28:29] neg_lo:[1,0,0] neg_hi:[1,0,0]
	v_pk_fma_f32 v[54:55], v[246:247], v[54:55], s[28:29] neg_lo:[1,0,0] neg_hi:[1,0,0]
	v_pk_mul_f32 v[48:49], v[228:229], v[48:49]
	v_pk_mul_f32 v[50:51], v[230:231], v[50:51]
	v_pk_mul_f32 v[52:53], v[244:245], v[52:53]
	v_pk_mul_f32 v[54:55], v[246:247], v[54:55]
	v_exp_f32_e32 v48, v48
	v_exp_f32_e32 v49, v49
	v_exp_f32_e32 v50, v50
	v_exp_f32_e32 v51, v51
	v_exp_f32_e32 v52, v52
	v_exp_f32_e32 v53, v53
	v_exp_f32_e32 v54, v54
	v_exp_f32_e32 v55, v55
	v_pk_add_f32 v[48:49], v[48:49], s[30:31]
	v_pk_add_f32 v[50:51], v[50:51], s[30:31]
	v_pk_add_f32 v[52:53], v[52:53], s[30:31]
	v_pk_add_f32 v[54:55], v[54:55], s[30:31]
	v_rcp_f32_e32 v48, v48
	v_rcp_f32_e32 v49, v49
	v_rcp_f32_e32 v50, v50
	v_rcp_f32_e32 v51, v51
	v_rcp_f32_e32 v52, v52
	v_rcp_f32_e32 v53, v53
	v_rcp_f32_e32 v54, v54
	v_rcp_f32_e32 v55, v55
	s_nop 0
	v_pk_mul_f32 v[228:229], v[228:229], v[48:49]
	v_pk_mul_f32 v[230:231], v[230:231], v[50:51]
	v_pk_mul_f32 v[244:245], v[244:245], v[52:53]
	v_pk_mul_f32 v[246:247], v[246:247], v[54:55]
	v_cvt_pk_bf16_f32 v68, v228, v229
	v_cvt_pk_bf16_f32 v69, v230, v231
	v_cvt_pk_bf16_f32 v70, v244, v245
	v_cvt_pk_bf16_f32 v71, v246, v247
	global_store_dwordx2 v17, v[68:69], s[10:11] offset:192
	global_store_dwordx2 v17, v[70:71], s[10:11] offset:224
	v_pk_mul_f32 v[136:137], v[136:137], v[24:25] op_sel_hi:[1,0]
	v_pk_mul_f32 v[138:139], v[138:139], v[24:25] op_sel_hi:[1,0]
	v_pk_mul_f32 v[152:153], v[152:153], v[24:25] op_sel_hi:[1,0]
	v_pk_mul_f32 v[154:155], v[154:155], v[24:25] op_sel_hi:[1,0]
	v_pk_mul_f32 v[32:33], v[136:137], s[26:27]
	v_pk_mul_f32 v[34:35], v[138:139], s[26:27]
	v_pk_mul_f32 v[36:37], v[152:153], s[26:27]
	v_pk_mul_f32 v[38:39], v[154:155], s[26:27]
	v_pk_fma_f32 v[32:33], v[136:137], v[32:33], s[28:29] neg_lo:[1,0,0] neg_hi:[1,0,0]
	v_pk_fma_f32 v[34:35], v[138:139], v[34:35], s[28:29] neg_lo:[1,0,0] neg_hi:[1,0,0]
	v_pk_fma_f32 v[36:37], v[152:153], v[36:37], s[28:29] neg_lo:[1,0,0] neg_hi:[1,0,0]
	v_pk_fma_f32 v[38:39], v[154:155], v[38:39], s[28:29] neg_lo:[1,0,0] neg_hi:[1,0,0]
	v_pk_mul_f32 v[32:33], v[136:137], v[32:33]
	v_pk_mul_f32 v[34:35], v[138:139], v[34:35]
	v_pk_mul_f32 v[36:37], v[152:153], v[36:37]
	v_pk_mul_f32 v[38:39], v[154:155], v[38:39]
	v_exp_f32_e32 v32, v32
	v_exp_f32_e32 v33, v33
	v_exp_f32_e32 v34, v34
	v_exp_f32_e32 v35, v35
	v_exp_f32_e32 v36, v36
	v_exp_f32_e32 v37, v37
	v_exp_f32_e32 v38, v38
	v_exp_f32_e32 v39, v39
	v_pk_add_f32 v[32:33], v[32:33], s[30:31]
	v_pk_add_f32 v[34:35], v[34:35], s[30:31]
	v_pk_add_f32 v[36:37], v[36:37], s[30:31]
	v_pk_add_f32 v[38:39], v[38:39], s[30:31]
	v_rcp_f32_e32 v32, v32
	v_rcp_f32_e32 v33, v33
	v_rcp_f32_e32 v34, v34
	v_rcp_f32_e32 v35, v35
	v_rcp_f32_e32 v36, v36
	v_rcp_f32_e32 v37, v37
	v_rcp_f32_e32 v38, v38
	v_rcp_f32_e32 v39, v39
	s_nop 0
	v_pk_mul_f32 v[136:137], v[136:137], v[32:33]
	v_pk_mul_f32 v[138:139], v[138:139], v[34:35]
	v_pk_mul_f32 v[152:153], v[152:153], v[36:37]
	v_pk_mul_f32 v[154:155], v[154:155], v[38:39]
	v_cvt_pk_bf16_f32 v64, v136, v137
	v_cvt_pk_bf16_f32 v65, v138, v139
	v_cvt_pk_bf16_f32 v66, v152, v153
	v_cvt_pk_bf16_f32 v67, v154, v155
	global_store_dwordx2 v18, v[64:65], s[10:11]
	global_store_dwordx2 v18, v[66:67], s[10:11] offset:32
	v_pk_mul_f32 v[168:169], v[168:169], v[24:25] op_sel_hi:[1,0]
	v_pk_mul_f32 v[170:171], v[170:171], v[24:25] op_sel_hi:[1,0]
	v_pk_mul_f32 v[184:185], v[184:185], v[24:25] op_sel_hi:[1,0]
	v_pk_mul_f32 v[186:187], v[186:187], v[24:25] op_sel_hi:[1,0]
	v_pk_mul_f32 v[48:49], v[168:169], s[26:27]
	v_pk_mul_f32 v[50:51], v[170:171], s[26:27]
	v_pk_mul_f32 v[52:53], v[184:185], s[26:27]
	v_pk_mul_f32 v[54:55], v[186:187], s[26:27]
	v_pk_fma_f32 v[48:49], v[168:169], v[48:49], s[28:29] neg_lo:[1,0,0] neg_hi:[1,0,0]
	v_pk_fma_f32 v[50:51], v[170:171], v[50:51], s[28:29] neg_lo:[1,0,0] neg_hi:[1,0,0]
	v_pk_fma_f32 v[52:53], v[184:185], v[52:53], s[28:29] neg_lo:[1,0,0] neg_hi:[1,0,0]
	v_pk_fma_f32 v[54:55], v[186:187], v[54:55], s[28:29] neg_lo:[1,0,0] neg_hi:[1,0,0]
	v_pk_mul_f32 v[48:49], v[168:169], v[48:49]
	v_pk_mul_f32 v[50:51], v[170:171], v[50:51]
	v_pk_mul_f32 v[52:53], v[184:185], v[52:53]
	v_pk_mul_f32 v[54:55], v[186:187], v[54:55]
	v_exp_f32_e32 v48, v48
	v_exp_f32_e32 v49, v49
	v_exp_f32_e32 v50, v50
	v_exp_f32_e32 v51, v51
	v_exp_f32_e32 v52, v52
	v_exp_f32_e32 v53, v53
	v_exp_f32_e32 v54, v54
	v_exp_f32_e32 v55, v55
	v_pk_add_f32 v[48:49], v[48:49], s[30:31]
	v_pk_add_f32 v[50:51], v[50:51], s[30:31]
	v_pk_add_f32 v[52:53], v[52:53], s[30:31]
	v_pk_add_f32 v[54:55], v[54:55], s[30:31]
	v_rcp_f32_e32 v48, v48
	v_rcp_f32_e32 v49, v49
	v_rcp_f32_e32 v50, v50
	v_rcp_f32_e32 v51, v51
	v_rcp_f32_e32 v52, v52
	v_rcp_f32_e32 v53, v53
	v_rcp_f32_e32 v54, v54
	v_rcp_f32_e32 v55, v55
	s_nop 0
	v_pk_mul_f32 v[168:169], v[168:169], v[48:49]
	v_pk_mul_f32 v[170:171], v[170:171], v[50:51]
	v_pk_mul_f32 v[184:185], v[184:185], v[52:53]
	v_pk_mul_f32 v[186:187], v[186:187], v[54:55]
	v_cvt_pk_bf16_f32 v68, v168, v169
	v_cvt_pk_bf16_f32 v69, v170, v171
	v_cvt_pk_bf16_f32 v70, v184, v185
	v_cvt_pk_bf16_f32 v71, v186, v187
	global_store_dwordx2 v18, v[68:69], s[10:11] offset:64
	global_store_dwordx2 v18, v[70:71], s[10:11] offset:96
	v_pk_mul_f32 v[200:201], v[200:201], v[24:25] op_sel_hi:[1,0]
	v_pk_mul_f32 v[202:203], v[202:203], v[24:25] op_sel_hi:[1,0]
	v_pk_mul_f32 v[216:217], v[216:217], v[24:25] op_sel_hi:[1,0]
	v_pk_mul_f32 v[218:219], v[218:219], v[24:25] op_sel_hi:[1,0]
	v_pk_mul_f32 v[32:33], v[200:201], s[26:27]
	v_pk_mul_f32 v[34:35], v[202:203], s[26:27]
	v_pk_mul_f32 v[36:37], v[216:217], s[26:27]
	v_pk_mul_f32 v[38:39], v[218:219], s[26:27]
	v_pk_fma_f32 v[32:33], v[200:201], v[32:33], s[28:29] neg_lo:[1,0,0] neg_hi:[1,0,0]
	v_pk_fma_f32 v[34:35], v[202:203], v[34:35], s[28:29] neg_lo:[1,0,0] neg_hi:[1,0,0]
	v_pk_fma_f32 v[36:37], v[216:217], v[36:37], s[28:29] neg_lo:[1,0,0] neg_hi:[1,0,0]
	v_pk_fma_f32 v[38:39], v[218:219], v[38:39], s[28:29] neg_lo:[1,0,0] neg_hi:[1,0,0]
	v_pk_mul_f32 v[32:33], v[200:201], v[32:33]
	v_pk_mul_f32 v[34:35], v[202:203], v[34:35]
	v_pk_mul_f32 v[36:37], v[216:217], v[36:37]
	v_pk_mul_f32 v[38:39], v[218:219], v[38:39]
	v_exp_f32_e32 v32, v32
	v_exp_f32_e32 v33, v33
	v_exp_f32_e32 v34, v34
	v_exp_f32_e32 v35, v35
	v_exp_f32_e32 v36, v36
	v_exp_f32_e32 v37, v37
	v_exp_f32_e32 v38, v38
	v_exp_f32_e32 v39, v39
	v_pk_add_f32 v[32:33], v[32:33], s[30:31]
	v_pk_add_f32 v[34:35], v[34:35], s[30:31]
	v_pk_add_f32 v[36:37], v[36:37], s[30:31]
	v_pk_add_f32 v[38:39], v[38:39], s[30:31]
	v_rcp_f32_e32 v32, v32
	v_rcp_f32_e32 v33, v33
	v_rcp_f32_e32 v34, v34
	v_rcp_f32_e32 v35, v35
	v_rcp_f32_e32 v36, v36
	v_rcp_f32_e32 v37, v37
	v_rcp_f32_e32 v38, v38
	v_rcp_f32_e32 v39, v39
	s_nop 0
	v_pk_mul_f32 v[200:201], v[200:201], v[32:33]
	v_pk_mul_f32 v[202:203], v[202:203], v[34:35]
	v_pk_mul_f32 v[216:217], v[216:217], v[36:37]
	v_pk_mul_f32 v[218:219], v[218:219], v[38:39]
	v_cvt_pk_bf16_f32 v64, v200, v201
	v_cvt_pk_bf16_f32 v65, v202, v203
	v_cvt_pk_bf16_f32 v66, v216, v217
	v_cvt_pk_bf16_f32 v67, v218, v219
	global_store_dwordx2 v18, v[64:65], s[10:11] offset:128
	global_store_dwordx2 v18, v[66:67], s[10:11] offset:160
	v_pk_mul_f32 v[232:233], v[232:233], v[24:25] op_sel_hi:[1,0]
	v_pk_mul_f32 v[234:235], v[234:235], v[24:25] op_sel_hi:[1,0]
	v_pk_mul_f32 v[248:249], v[248:249], v[24:25] op_sel_hi:[1,0]
	v_pk_mul_f32 v[250:251], v[250:251], v[24:25] op_sel_hi:[1,0]
	v_pk_mul_f32 v[48:49], v[232:233], s[26:27]
	v_pk_mul_f32 v[50:51], v[234:235], s[26:27]
	v_pk_mul_f32 v[52:53], v[248:249], s[26:27]
	v_pk_mul_f32 v[54:55], v[250:251], s[26:27]
	v_pk_fma_f32 v[48:49], v[232:233], v[48:49], s[28:29] neg_lo:[1,0,0] neg_hi:[1,0,0]
	v_pk_fma_f32 v[50:51], v[234:235], v[50:51], s[28:29] neg_lo:[1,0,0] neg_hi:[1,0,0]
	v_pk_fma_f32 v[52:53], v[248:249], v[52:53], s[28:29] neg_lo:[1,0,0] neg_hi:[1,0,0]
	v_pk_fma_f32 v[54:55], v[250:251], v[54:55], s[28:29] neg_lo:[1,0,0] neg_hi:[1,0,0]
	v_pk_mul_f32 v[48:49], v[232:233], v[48:49]
	v_pk_mul_f32 v[50:51], v[234:235], v[50:51]
	v_pk_mul_f32 v[52:53], v[248:249], v[52:53]
	v_pk_mul_f32 v[54:55], v[250:251], v[54:55]
	v_exp_f32_e32 v48, v48
	v_exp_f32_e32 v49, v49
	v_exp_f32_e32 v50, v50
	v_exp_f32_e32 v51, v51
	v_exp_f32_e32 v52, v52
	v_exp_f32_e32 v53, v53
	v_exp_f32_e32 v54, v54
	v_exp_f32_e32 v55, v55
	v_pk_add_f32 v[48:49], v[48:49], s[30:31]
	v_pk_add_f32 v[50:51], v[50:51], s[30:31]
	v_pk_add_f32 v[52:53], v[52:53], s[30:31]
	v_pk_add_f32 v[54:55], v[54:55], s[30:31]
	v_rcp_f32_e32 v48, v48
	v_rcp_f32_e32 v49, v49
	v_rcp_f32_e32 v50, v50
	v_rcp_f32_e32 v51, v51
	v_rcp_f32_e32 v52, v52
	v_rcp_f32_e32 v53, v53
	v_rcp_f32_e32 v54, v54
	v_rcp_f32_e32 v55, v55
	s_nop 0
	v_pk_mul_f32 v[232:233], v[232:233], v[48:49]
	v_pk_mul_f32 v[234:235], v[234:235], v[50:51]
	v_pk_mul_f32 v[248:249], v[248:249], v[52:53]
	v_pk_mul_f32 v[250:251], v[250:251], v[54:55]
	v_cvt_pk_bf16_f32 v68, v232, v233
	v_cvt_pk_bf16_f32 v69, v234, v235
	v_cvt_pk_bf16_f32 v70, v248, v249
	v_cvt_pk_bf16_f32 v71, v250, v251
	global_store_dwordx2 v18, v[68:69], s[10:11] offset:192
	global_store_dwordx2 v18, v[70:71], s[10:11] offset:224
	v_pk_mul_f32 v[140:141], v[140:141], v[26:27] op_sel_hi:[1,0]
	v_pk_mul_f32 v[142:143], v[142:143], v[26:27] op_sel_hi:[1,0]
	v_pk_mul_f32 v[156:157], v[156:157], v[26:27] op_sel_hi:[1,0]
	v_pk_mul_f32 v[158:159], v[158:159], v[26:27] op_sel_hi:[1,0]
	v_pk_mul_f32 v[32:33], v[140:141], s[26:27]
	v_pk_mul_f32 v[34:35], v[142:143], s[26:27]
	v_pk_mul_f32 v[36:37], v[156:157], s[26:27]
	v_pk_mul_f32 v[38:39], v[158:159], s[26:27]
	v_pk_fma_f32 v[32:33], v[140:141], v[32:33], s[28:29] neg_lo:[1,0,0] neg_hi:[1,0,0]
	v_pk_fma_f32 v[34:35], v[142:143], v[34:35], s[28:29] neg_lo:[1,0,0] neg_hi:[1,0,0]
	v_pk_fma_f32 v[36:37], v[156:157], v[36:37], s[28:29] neg_lo:[1,0,0] neg_hi:[1,0,0]
	v_pk_fma_f32 v[38:39], v[158:159], v[38:39], s[28:29] neg_lo:[1,0,0] neg_hi:[1,0,0]
	v_pk_mul_f32 v[32:33], v[140:141], v[32:33]
	v_pk_mul_f32 v[34:35], v[142:143], v[34:35]
	v_pk_mul_f32 v[36:37], v[156:157], v[36:37]
	v_pk_mul_f32 v[38:39], v[158:159], v[38:39]
	v_exp_f32_e32 v32, v32
	v_exp_f32_e32 v33, v33
	v_exp_f32_e32 v34, v34
	v_exp_f32_e32 v35, v35
	v_exp_f32_e32 v36, v36
	v_exp_f32_e32 v37, v37
	v_exp_f32_e32 v38, v38
	v_exp_f32_e32 v39, v39
	v_pk_add_f32 v[32:33], v[32:33], s[30:31]
	v_pk_add_f32 v[34:35], v[34:35], s[30:31]
	v_pk_add_f32 v[36:37], v[36:37], s[30:31]
	v_pk_add_f32 v[38:39], v[38:39], s[30:31]
	v_rcp_f32_e32 v32, v32
	v_rcp_f32_e32 v33, v33
	v_rcp_f32_e32 v34, v34
	v_rcp_f32_e32 v35, v35
	v_rcp_f32_e32 v36, v36
	v_rcp_f32_e32 v37, v37
	v_rcp_f32_e32 v38, v38
	v_rcp_f32_e32 v39, v39
	s_nop 0
	v_pk_mul_f32 v[140:141], v[140:141], v[32:33]
	v_pk_mul_f32 v[142:143], v[142:143], v[34:35]
	v_pk_mul_f32 v[156:157], v[156:157], v[36:37]
	v_pk_mul_f32 v[158:159], v[158:159], v[38:39]
	v_cvt_pk_bf16_f32 v64, v140, v141
	v_cvt_pk_bf16_f32 v65, v142, v143
	v_cvt_pk_bf16_f32 v66, v156, v157
	v_cvt_pk_bf16_f32 v67, v158, v159
	global_store_dwordx2 v19, v[64:65], s[10:11]
	global_store_dwordx2 v19, v[66:67], s[10:11] offset:32
	v_pk_mul_f32 v[172:173], v[172:173], v[26:27] op_sel_hi:[1,0]
	v_pk_mul_f32 v[174:175], v[174:175], v[26:27] op_sel_hi:[1,0]
	v_pk_mul_f32 v[188:189], v[188:189], v[26:27] op_sel_hi:[1,0]
	v_pk_mul_f32 v[190:191], v[190:191], v[26:27] op_sel_hi:[1,0]
	v_pk_mul_f32 v[48:49], v[172:173], s[26:27]
	v_pk_mul_f32 v[50:51], v[174:175], s[26:27]
	v_pk_mul_f32 v[52:53], v[188:189], s[26:27]
	v_pk_mul_f32 v[54:55], v[190:191], s[26:27]
	v_pk_fma_f32 v[48:49], v[172:173], v[48:49], s[28:29] neg_lo:[1,0,0] neg_hi:[1,0,0]
	v_pk_fma_f32 v[50:51], v[174:175], v[50:51], s[28:29] neg_lo:[1,0,0] neg_hi:[1,0,0]
	v_pk_fma_f32 v[52:53], v[188:189], v[52:53], s[28:29] neg_lo:[1,0,0] neg_hi:[1,0,0]
	v_pk_fma_f32 v[54:55], v[190:191], v[54:55], s[28:29] neg_lo:[1,0,0] neg_hi:[1,0,0]
	v_pk_mul_f32 v[48:49], v[172:173], v[48:49]
	v_pk_mul_f32 v[50:51], v[174:175], v[50:51]
	v_pk_mul_f32 v[52:53], v[188:189], v[52:53]
	v_pk_mul_f32 v[54:55], v[190:191], v[54:55]
	v_exp_f32_e32 v48, v48
	v_exp_f32_e32 v49, v49
	v_exp_f32_e32 v50, v50
	v_exp_f32_e32 v51, v51
	v_exp_f32_e32 v52, v52
	v_exp_f32_e32 v53, v53
	v_exp_f32_e32 v54, v54
	v_exp_f32_e32 v55, v55
	v_pk_add_f32 v[48:49], v[48:49], s[30:31]
	v_pk_add_f32 v[50:51], v[50:51], s[30:31]
	v_pk_add_f32 v[52:53], v[52:53], s[30:31]
	v_pk_add_f32 v[54:55], v[54:55], s[30:31]
	v_rcp_f32_e32 v48, v48
	v_rcp_f32_e32 v49, v49
	v_rcp_f32_e32 v50, v50
	v_rcp_f32_e32 v51, v51
	v_rcp_f32_e32 v52, v52
	v_rcp_f32_e32 v53, v53
	v_rcp_f32_e32 v54, v54
	v_rcp_f32_e32 v55, v55
	s_nop 0
	v_pk_mul_f32 v[172:173], v[172:173], v[48:49]
	v_pk_mul_f32 v[174:175], v[174:175], v[50:51]
	v_pk_mul_f32 v[188:189], v[188:189], v[52:53]
	v_pk_mul_f32 v[190:191], v[190:191], v[54:55]
	v_cvt_pk_bf16_f32 v68, v172, v173
	v_cvt_pk_bf16_f32 v69, v174, v175
	v_cvt_pk_bf16_f32 v70, v188, v189
	v_cvt_pk_bf16_f32 v71, v190, v191
	global_store_dwordx2 v19, v[68:69], s[10:11] offset:64
	global_store_dwordx2 v19, v[70:71], s[10:11] offset:96
	v_pk_mul_f32 v[204:205], v[204:205], v[26:27] op_sel_hi:[1,0]
	v_pk_mul_f32 v[206:207], v[206:207], v[26:27] op_sel_hi:[1,0]
	v_pk_mul_f32 v[220:221], v[220:221], v[26:27] op_sel_hi:[1,0]
	v_pk_mul_f32 v[222:223], v[222:223], v[26:27] op_sel_hi:[1,0]
	v_pk_mul_f32 v[32:33], v[204:205], s[26:27]
	v_pk_mul_f32 v[34:35], v[206:207], s[26:27]
	v_pk_mul_f32 v[36:37], v[220:221], s[26:27]
	v_pk_mul_f32 v[38:39], v[222:223], s[26:27]
	v_pk_fma_f32 v[32:33], v[204:205], v[32:33], s[28:29] neg_lo:[1,0,0] neg_hi:[1,0,0]
	v_pk_fma_f32 v[34:35], v[206:207], v[34:35], s[28:29] neg_lo:[1,0,0] neg_hi:[1,0,0]
	v_pk_fma_f32 v[36:37], v[220:221], v[36:37], s[28:29] neg_lo:[1,0,0] neg_hi:[1,0,0]
	v_pk_fma_f32 v[38:39], v[222:223], v[38:39], s[28:29] neg_lo:[1,0,0] neg_hi:[1,0,0]
	v_pk_mul_f32 v[32:33], v[204:205], v[32:33]
	v_pk_mul_f32 v[34:35], v[206:207], v[34:35]
	v_pk_mul_f32 v[36:37], v[220:221], v[36:37]
	v_pk_mul_f32 v[38:39], v[222:223], v[38:39]
	v_exp_f32_e32 v32, v32
	v_exp_f32_e32 v33, v33
	v_exp_f32_e32 v34, v34
	v_exp_f32_e32 v35, v35
	v_exp_f32_e32 v36, v36
	v_exp_f32_e32 v37, v37
	v_exp_f32_e32 v38, v38
	v_exp_f32_e32 v39, v39
	v_pk_add_f32 v[32:33], v[32:33], s[30:31]
	v_pk_add_f32 v[34:35], v[34:35], s[30:31]
	v_pk_add_f32 v[36:37], v[36:37], s[30:31]
	v_pk_add_f32 v[38:39], v[38:39], s[30:31]
	v_rcp_f32_e32 v32, v32
	v_rcp_f32_e32 v33, v33
	v_rcp_f32_e32 v34, v34
	v_rcp_f32_e32 v35, v35
	v_rcp_f32_e32 v36, v36
	v_rcp_f32_e32 v37, v37
	v_rcp_f32_e32 v38, v38
	v_rcp_f32_e32 v39, v39
	s_nop 0
	v_pk_mul_f32 v[204:205], v[204:205], v[32:33]
	v_pk_mul_f32 v[206:207], v[206:207], v[34:35]
	v_pk_mul_f32 v[220:221], v[220:221], v[36:37]
	v_pk_mul_f32 v[222:223], v[222:223], v[38:39]
	v_cvt_pk_bf16_f32 v64, v204, v205
	v_cvt_pk_bf16_f32 v65, v206, v207
	v_cvt_pk_bf16_f32 v66, v220, v221
	v_cvt_pk_bf16_f32 v67, v222, v223
	global_store_dwordx2 v19, v[64:65], s[10:11] offset:128
	global_store_dwordx2 v19, v[66:67], s[10:11] offset:160
	v_pk_mul_f32 v[236:237], v[236:237], v[26:27] op_sel_hi:[1,0]
	v_pk_mul_f32 v[238:239], v[238:239], v[26:27] op_sel_hi:[1,0]
	v_pk_mul_f32 v[252:253], v[252:253], v[26:27] op_sel_hi:[1,0]
	v_pk_mul_f32 v[254:255], v[254:255], v[26:27] op_sel_hi:[1,0]
	v_pk_mul_f32 v[48:49], v[236:237], s[26:27]
	v_pk_mul_f32 v[50:51], v[238:239], s[26:27]
	v_pk_mul_f32 v[52:53], v[252:253], s[26:27]
	v_pk_mul_f32 v[54:55], v[254:255], s[26:27]
	v_pk_fma_f32 v[48:49], v[236:237], v[48:49], s[28:29] neg_lo:[1,0,0] neg_hi:[1,0,0]
	v_pk_fma_f32 v[50:51], v[238:239], v[50:51], s[28:29] neg_lo:[1,0,0] neg_hi:[1,0,0]
	v_pk_fma_f32 v[52:53], v[252:253], v[52:53], s[28:29] neg_lo:[1,0,0] neg_hi:[1,0,0]
	v_pk_fma_f32 v[54:55], v[254:255], v[54:55], s[28:29] neg_lo:[1,0,0] neg_hi:[1,0,0]
	v_pk_mul_f32 v[48:49], v[236:237], v[48:49]
	v_pk_mul_f32 v[50:51], v[238:239], v[50:51]
	v_pk_mul_f32 v[52:53], v[252:253], v[52:53]
	v_pk_mul_f32 v[54:55], v[254:255], v[54:55]
	v_exp_f32_e32 v48, v48
	v_exp_f32_e32 v49, v49
	v_exp_f32_e32 v50, v50
	v_exp_f32_e32 v51, v51
	v_exp_f32_e32 v52, v52
	v_exp_f32_e32 v53, v53
	v_exp_f32_e32 v54, v54
	v_exp_f32_e32 v55, v55
	v_pk_add_f32 v[48:49], v[48:49], s[30:31]
	v_pk_add_f32 v[50:51], v[50:51], s[30:31]
	v_pk_add_f32 v[52:53], v[52:53], s[30:31]
	v_pk_add_f32 v[54:55], v[54:55], s[30:31]
	v_rcp_f32_e32 v48, v48
	v_rcp_f32_e32 v49, v49
	v_rcp_f32_e32 v50, v50
	v_rcp_f32_e32 v51, v51
	v_rcp_f32_e32 v52, v52
	v_rcp_f32_e32 v53, v53
	v_rcp_f32_e32 v54, v54
	v_rcp_f32_e32 v55, v55
	s_nop 0
	v_pk_mul_f32 v[236:237], v[236:237], v[48:49]
	v_pk_mul_f32 v[238:239], v[238:239], v[50:51]
	v_pk_mul_f32 v[252:253], v[252:253], v[52:53]
	v_pk_mul_f32 v[254:255], v[254:255], v[54:55]
	v_cvt_pk_bf16_f32 v68, v236, v237
	v_cvt_pk_bf16_f32 v69, v238, v239
	v_cvt_pk_bf16_f32 v70, v252, v253
	v_cvt_pk_bf16_f32 v71, v254, v255
	global_store_dwordx2 v19, v[68:69], s[10:11] offset:192
	global_store_dwordx2 v19, v[70:71], s[10:11] offset:224
